# final RMSNorm hand-pipelined + kv-GEMM epilogue: 8 sum-of-squares loads issued together (one wait) instead of 4 serialized rounds
# baseline (speedup 1.0000x reference)
.LBB0_860:
	s_ashr_i32 s5, s4, 31
	s_lshl_b64 s[0:1], s[4:5], 8
	s_add_u32 s42, s0, s68
	s_addc_u32 s43, s1, s76
	v_mov_b32_e32 v209, v201
	v_mov_b32_e32 v2, v206
	s_lshl_b64 s[0:1], s[42:43], 6
	v_readlane_b32 s4, v251, 42
	s_add_u32 s0, s4, s0
	v_readlane_b32 s4, v251, 43
	v_lshlrev_b32_e32 v3, 6, v209
	s_addc_u32 s1, s4, s1
	v_lshl_add_u32 v202, v2, 4, v3
	v_cmp_lt_i32_e64 s[4:5], 0, v2
	v_cmp_gt_i32_e32 vcc, 1, v2
	v_lshl_add_u64 v[194:195], s[0:1], 0, v[202:203]
	v_mov_b32_e32 v2, 0
	v_mov_b32_e32 v3, 0
	v_mov_b32_e32 v4, 0
	v_mov_b32_e32 v5, 0
	v_mov_b32_e32 v6, 0
	v_mov_b32_e32 v7, 0
	v_mov_b32_e32 v8, 0
	v_mov_b32_e32 v9, 0
	v_mov_b32_e32 v10, 0
	v_mov_b32_e32 v11, 0
	v_mov_b32_e32 v12, 0
	v_mov_b32_e32 v13, 0
	v_mov_b32_e32 v14, 0
	v_mov_b32_e32 v15, 0
	v_mov_b32_e32 v16, 0
	v_mov_b32_e32 v17, 0
	v_mov_b32_e32 v18, 0
	v_mov_b32_e32 v19, 0
	v_mov_b32_e32 v20, 0
	v_mov_b32_e32 v21, 0
	v_mov_b32_e32 v22, 0
	v_mov_b32_e32 v23, 0
	v_mov_b32_e32 v24, 0
	v_mov_b32_e32 v25, 0
	v_mov_b32_e32 v26, 0
	v_mov_b32_e32 v27, 0
	v_mov_b32_e32 v28, 0
	v_mov_b32_e32 v29, 0
	v_mov_b32_e32 v30, 0
	v_mov_b32_e32 v31, 0
	v_mov_b32_e32 v32, 0
	v_mov_b32_e32 v33, 0
	s_and_saveexec_b64 s[44:45], vcc
	s_cbranch_execz .Lkv_ss_done
	global_load_dwordx4 v[2:5], v[194:195], off offset:32
	global_load_dwordx4 v[6:9], v[194:195], off offset:1056
	global_load_dwordx4 v[10:13], v[194:195], off offset:2080
	global_load_dwordx4 v[14:17], v[194:195], off offset:3104
	s_mov_b64 s[0:1], 0x2020
	v_lshl_add_u64 v[34:35], s[0:1], 0, v[194:195]
	global_load_dwordx4 v[18:21], v[34:35], off
	global_load_dwordx4 v[22:25], v[34:35], off offset:1024
	global_load_dwordx4 v[26:29], v[34:35], off offset:2048
	global_load_dwordx4 v[30:33], v[34:35], off offset:3072
.Lkv_ss_done:
	s_or_b64 exec, exec, s[44:45]
	s_waitcnt vmcnt(0)
.LBB0_868:
	s_or_b64 exec, exec, s[4:5]
	v_and_b32_e32 v35, 64, v248
	v_xor_b32_e32 v34, 16, v248
	v_add_u32_e32 v35, 64, v35
	v_cmp_lt_i32_e32 vcc, v34, v35
	v_mov_b32_e32 v40, v3
	v_mov_b32_e32 v41, v4
	v_mov_b32_e32 v3, v5
	v_cndmask_b32_e32 v34, v248, v34, vcc
	v_pk_add_f32 v[2:3], v[40:41], v[2:3]
	v_lshlrev_b32_e32 v37, 2, v34
	v_add_f32_e32 v2, v2, v3
	ds_bpermute_b32 v3, v37, v2
	v_xor_b32_e32 v34, 32, v248
	v_cmp_lt_i32_e32 vcc, v34, v35
	v_readlane_b32 s44, v249, 7
	s_mov_b32 s13, 0xf800000
	v_cndmask_b32_e32 v34, v248, v34, vcc
	v_lshlrev_b32_e32 v36, 2, v34
	s_waitcnt lgkmcnt(0)
	v_add_f32_e32 v2, v2, v3
	ds_bpermute_b32 v3, v36, v2
	s_movk_i32 s0, 0xfc0
	v_readlane_b32 s48, v249, 11
	v_readlane_b32 s49, v249, 12
	v_mad_u64_u32 v[38:39], s[0:1], v209, s0, v[202:203]
	s_waitcnt lgkmcnt(0)
	v_add_f32_e32 v2, v2, v3
	v_fmamk_f32 v2, v2, 0x3b800000, v204
	v_cmp_gt_f32_e32 vcc, s13, v2
	v_mul_f32_e32 v3, 0x4f800000, v2
	v_readlane_b32 s50, v249, 13
	v_readlane_b32 s51, v249, 14
	s_mov_b64 s[16:17], s[48:49]
	v_cndmask_b32_e32 v2, v2, v3, vcc
	s_lshl_b64 s[0:1], s[42:43], 12
	s_mov_b64 s[18:19], s[50:51]
	v_sqrt_f32_e32 v3, v2
	s_add_u32 s4, s18, s0
	s_addc_u32 s5, s19, s1
	s_lshl_b32 s0, s22, 8
	s_ashr_i32 s1, s0, 31
	s_lshl_b64 s[0:1], s[0:1], 1
	v_add_u32_e32 v4, -1, v3
	s_add_u32 s0, s4, s0
	v_fma_f32 v5, -v4, v3, v2
	s_addc_u32 s1, s5, s1
	v_cmp_ge_f32_e64 s[4:5], 0, v5
	v_add_u32_e32 v5, 1, v3
	s_add_u32 s22, s0, s78
	v_cndmask_b32_e64 v4, v3, v4, s[4:5]
	v_fma_f32 v3, -v5, v3, v2
	v_cmp_lt_f32_e64 s[4:5], 0, v3
	s_addc_u32 s23, s1, 0
	v_mov_b32_e32 v39, v203
	v_cndmask_b32_e64 v3, v4, v5, s[4:5]
	v_mul_f32_e32 v4, 0x37800000, v3
	v_cndmask_b32_e32 v3, v3, v4, vcc
	v_cmp_class_f32_e32 vcc, v2, v205
	v_lshl_add_u64 v[34:35], s[22:23], 0, v[38:39]
	s_mov_b32 s15, 0xf800000
	v_cndmask_b32_e32 v2, v3, v2, vcc
	v_div_scale_f32 v3, s[0:1], v2, v2, 1.0
	v_rcp_f32_e32 v4, v3
	v_readlane_b32 s45, v249, 8
	v_readlane_b32 s46, v249, 9
	v_readlane_b32 s47, v249, 10
	v_fma_f32 v5, -v3, v4, 1.0
	v_fmac_f32_e32 v4, v5, v4
	v_div_scale_f32 v5, vcc, 1.0, v2, 1.0
	v_mul_f32_e32 v39, v5, v4
	v_fma_f32 v40, -v3, v39, v5
	v_fmac_f32_e32 v39, v40, v4
	v_fma_f32 v3, -v3, v39, v5
	v_div_fmas_f32 v3, v3, v4, v39
	v_div_fixup_f32 v40, v3, v2, 1.0
	v_pk_mul_f32 v[2:3], v[190:191], v[40:41] op_sel_hi:[1,0]
	v_pk_mul_f32 v[4:5], v[192:193], v[40:41] op_sel_hi:[1,0]
	v_cvt_pk_bf16_f32 v2, v2, v3
	v_pk_mul_f32 v[42:43], v[188:189], v[40:41] op_sel_hi:[1,0]
	v_cvt_pk_bf16_f32 v3, v4, v5
	v_pk_mul_f32 v[44:45], v[186:187], v[40:41] op_sel_hi:[1,0]
	s_nop 0
	v_cvt_pk_bf16_f32 v4, v44, v45
	v_cvt_pk_bf16_f32 v5, v42, v43
	global_store_dwordx4 v38, v[2:5], s[22:23]
	v_pk_mul_f32 v[42:43], v[180:181], v[40:41] op_sel_hi:[1,0]
	s_nop 0
	v_pk_mul_f32 v[2:3], v[182:183], v[40:41] op_sel_hi:[1,0]
	v_pk_mul_f32 v[4:5], v[184:185], v[40:41] op_sel_hi:[1,0]
	v_cvt_pk_bf16_f32 v2, v2, v3
	v_pk_mul_f32 v[40:41], v[178:179], v[40:41] op_sel_hi:[1,0]
	v_cvt_pk_bf16_f32 v3, v4, v5
	s_nop 0
	v_cvt_pk_bf16_f32 v4, v40, v41
	v_cvt_pk_bf16_f32 v5, v42, v43
	global_store_dwordx4 v38, v[2:5], s[22:23] offset:256
	s_nop 1
	v_mov_b32_e32 v2, v7
	v_mov_b32_e32 v3, v8
	v_mov_b32_e32 v7, v9
	v_pk_add_f32 v[2:3], v[2:3], v[6:7]
	s_nop 0
	v_add_f32_e32 v2, v2, v3
	ds_bpermute_b32 v3, v37, v2
	s_waitcnt lgkmcnt(0)
	v_add_f32_e32 v2, v2, v3
	ds_bpermute_b32 v3, v36, v2
	s_waitcnt lgkmcnt(0)
	v_add_f32_e32 v2, v2, v3
	v_fmamk_f32 v2, v2, 0x3b800000, v204
	v_cmp_gt_f32_e32 vcc, s13, v2
	v_mul_f32_e32 v3, 0x4f800000, v2
	s_nop 0
	v_cndmask_b32_e32 v2, v2, v3, vcc
	v_sqrt_f32_e32 v3, v2
	s_nop 0
	v_add_u32_e32 v4, -1, v3
	v_fma_f32 v5, -v4, v3, v2
	v_cmp_ge_f32_e64 s[4:5], 0, v5
	v_add_u32_e32 v5, 1, v3
	s_nop 0
	v_cndmask_b32_e64 v4, v3, v4, s[4:5]
	v_fma_f32 v3, -v5, v3, v2
	v_cmp_lt_f32_e64 s[4:5], 0, v3
	s_nop 1
	v_cndmask_b32_e64 v3, v4, v5, s[4:5]
	v_mul_f32_e32 v4, 0x37800000, v3
	v_cndmask_b32_e32 v3, v3, v4, vcc
	v_cmp_class_f32_e32 vcc, v2, v205
	s_nop 1
	v_cndmask_b32_e32 v2, v3, v2, vcc
	v_div_scale_f32 v3, s[0:1], v2, v2, 1.0
	v_rcp_f32_e32 v4, v3
	s_mov_b32 s0, 0x10000
	v_fma_f32 v5, -v3, v4, 1.0
	v_fmac_f32_e32 v4, v5, v4
	v_div_scale_f32 v5, vcc, 1.0, v2, 1.0
	v_mul_f32_e32 v6, v5, v4
	v_fma_f32 v7, -v3, v6, v5
	v_fmac_f32_e32 v6, v7, v4
	v_fma_f32 v3, -v3, v6, v5
	v_div_fmas_f32 v3, v3, v4, v6
	v_div_fixup_f32 v6, v3, v2, 1.0
	v_pk_mul_f32 v[4:5], v[176:177], v[6:7] op_sel_hi:[1,0]
	v_pk_mul_f32 v[2:3], v[174:175], v[6:7] op_sel_hi:[1,0]
	v_pk_mul_f32 v[8:9], v[172:173], v[6:7] op_sel_hi:[1,0]
	v_pk_mul_f32 v[38:39], v[170:171], v[6:7] op_sel_hi:[1,0]
	v_cvt_pk_bf16_f32 v2, v2, v3
	v_cvt_pk_bf16_f32 v3, v4, v5
	s_nop 0
	v_cvt_pk_bf16_f32 v4, v38, v39
	v_cvt_pk_bf16_f32 v5, v8, v9
	v_add_co_u32_e32 v8, vcc, s0, v34
	v_pk_mul_f32 v[38:39], v[164:165], v[6:7] op_sel_hi:[1,0]
	s_nop 0
	v_addc_co_u32_e32 v9, vcc, 0, v35, vcc
	global_store_dwordx4 v[8:9], v[2:5], off
	s_nop 1
	v_pk_mul_f32 v[2:3], v[166:167], v[6:7] op_sel_hi:[1,0]
	v_pk_mul_f32 v[4:5], v[168:169], v[6:7] op_sel_hi:[1,0]
	v_cvt_pk_bf16_f32 v2, v2, v3
	v_pk_mul_f32 v[6:7], v[162:163], v[6:7] op_sel_hi:[1,0]
	v_cvt_pk_bf16_f32 v3, v4, v5
	s_nop 0
	v_cvt_pk_bf16_f32 v4, v6, v7
	v_cvt_pk_bf16_f32 v5, v38, v39
	global_store_dwordx4 v[8:9], v[2:5], off offset:256
	s_nop 1
	v_mov_b32_e32 v2, v11
	v_mov_b32_e32 v3, v12
	v_mov_b32_e32 v11, v13
	v_pk_add_f32 v[2:3], v[2:3], v[10:11]
	s_nop 0
	v_add_f32_e32 v2, v2, v3
	ds_bpermute_b32 v3, v37, v2
	s_waitcnt lgkmcnt(0)
	v_add_f32_e32 v2, v2, v3
	ds_bpermute_b32 v3, v36, v2
	s_waitcnt lgkmcnt(0)
	v_add_f32_e32 v2, v2, v3
	v_fmamk_f32 v2, v2, 0x3b800000, v204
	v_cmp_gt_f32_e32 vcc, s13, v2
	v_mul_f32_e32 v3, 0x4f800000, v2
	s_nop 0
	v_cndmask_b32_e32 v2, v2, v3, vcc
	v_sqrt_f32_e32 v3, v2
	s_nop 0
	v_add_u32_e32 v4, -1, v3
	v_fma_f32 v5, -v4, v3, v2
	v_cmp_ge_f32_e64 s[4:5], 0, v5
	v_add_u32_e32 v5, 1, v3
	s_nop 0
	v_cndmask_b32_e64 v4, v3, v4, s[4:5]
	v_fma_f32 v3, -v5, v3, v2
	v_cmp_lt_f32_e64 s[4:5], 0, v3
	s_nop 1
	v_cndmask_b32_e64 v3, v4, v5, s[4:5]
	v_mul_f32_e32 v4, 0x37800000, v3
	v_cndmask_b32_e32 v3, v3, v4, vcc
	v_cmp_class_f32_e32 vcc, v2, v205
	s_nop 1
	v_cndmask_b32_e32 v2, v3, v2, vcc
	v_div_scale_f32 v3, s[0:1], v2, v2, 1.0
	v_rcp_f32_e32 v4, v3
	s_mov_b32 s0, 0x20000
	v_fma_f32 v5, -v3, v4, 1.0
	v_fmac_f32_e32 v4, v5, v4
	v_div_scale_f32 v5, vcc, 1.0, v2, 1.0
	v_mul_f32_e32 v6, v5, v4
	v_fma_f32 v7, -v3, v6, v5
	v_fmac_f32_e32 v6, v7, v4
	v_fma_f32 v3, -v3, v6, v5
	v_div_fmas_f32 v3, v3, v4, v6
	v_div_fixup_f32 v6, v3, v2, 1.0
	v_pk_mul_f32 v[4:5], v[160:161], v[6:7] op_sel_hi:[1,0]
	v_pk_mul_f32 v[2:3], v[158:159], v[6:7] op_sel_hi:[1,0]
	v_pk_mul_f32 v[8:9], v[156:157], v[6:7] op_sel_hi:[1,0]
	v_pk_mul_f32 v[10:11], v[154:155], v[6:7] op_sel_hi:[1,0]
	v_cvt_pk_bf16_f32 v2, v2, v3
	v_cvt_pk_bf16_f32 v3, v4, v5
	s_nop 0
	v_cvt_pk_bf16_f32 v4, v10, v11
	v_cvt_pk_bf16_f32 v5, v8, v9
	v_add_co_u32_e32 v8, vcc, s0, v34
	v_pk_mul_f32 v[10:11], v[148:149], v[6:7] op_sel_hi:[1,0]
	s_nop 0
	v_addc_co_u32_e32 v9, vcc, 0, v35, vcc
	global_store_dwordx4 v[8:9], v[2:5], off
	s_nop 1
	v_pk_mul_f32 v[2:3], v[150:151], v[6:7] op_sel_hi:[1,0]
	v_pk_mul_f32 v[4:5], v[152:153], v[6:7] op_sel_hi:[1,0]
	v_cvt_pk_bf16_f32 v2, v2, v3
	v_pk_mul_f32 v[6:7], v[146:147], v[6:7] op_sel_hi:[1,0]
	v_cvt_pk_bf16_f32 v3, v4, v5
	s_nop 0
	v_cvt_pk_bf16_f32 v4, v6, v7
	v_cvt_pk_bf16_f32 v5, v10, v11
	global_store_dwordx4 v[8:9], v[2:5], off offset:256
	s_nop 1
	v_mov_b32_e32 v2, v15
	v_mov_b32_e32 v3, v16
	v_mov_b32_e32 v15, v17
	v_pk_add_f32 v[2:3], v[2:3], v[14:15]
	s_nop 0
	v_add_f32_e32 v2, v2, v3
	ds_bpermute_b32 v3, v37, v2
	s_waitcnt lgkmcnt(0)
	v_add_f32_e32 v2, v2, v3
	ds_bpermute_b32 v3, v36, v2
	s_waitcnt lgkmcnt(0)
	v_add_f32_e32 v2, v2, v3
	v_fmamk_f32 v2, v2, 0x3b800000, v204
	v_cmp_gt_f32_e32 vcc, s13, v2
	v_mul_f32_e32 v3, 0x4f800000, v2
	s_nop 0
	v_cndmask_b32_e32 v2, v2, v3, vcc
	v_sqrt_f32_e32 v3, v2
	s_nop 0
	v_add_u32_e32 v4, -1, v3
	v_fma_f32 v5, -v4, v3, v2
	v_cmp_ge_f32_e64 s[4:5], 0, v5
	v_add_u32_e32 v5, 1, v3
	s_nop 0
	v_cndmask_b32_e64 v4, v3, v4, s[4:5]
	v_fma_f32 v3, -v5, v3, v2
	v_cmp_lt_f32_e64 s[4:5], 0, v3
	s_nop 1
	v_cndmask_b32_e64 v3, v4, v5, s[4:5]
	v_mul_f32_e32 v4, 0x37800000, v3
	v_cndmask_b32_e32 v3, v3, v4, vcc
	v_cmp_class_f32_e32 vcc, v2, v205
	s_nop 1
	v_cndmask_b32_e32 v2, v3, v2, vcc
	v_div_scale_f32 v3, s[0:1], v2, v2, 1.0
	v_rcp_f32_e32 v4, v3
	s_mov_b32 s0, 0x30000
	v_fma_f32 v5, -v3, v4, 1.0
	v_fmac_f32_e32 v4, v5, v4
	v_div_scale_f32 v5, vcc, 1.0, v2, 1.0
	v_mul_f32_e32 v6, v5, v4
	v_fma_f32 v7, -v3, v6, v5
	v_fmac_f32_e32 v6, v7, v4
	v_fma_f32 v3, -v3, v6, v5
	v_div_fmas_f32 v3, v3, v4, v6
	v_div_fixup_f32 v6, v3, v2, 1.0
	v_pk_mul_f32 v[4:5], v[144:145], v[6:7] op_sel_hi:[1,0]
	v_pk_mul_f32 v[2:3], v[142:143], v[6:7] op_sel_hi:[1,0]
	v_pk_mul_f32 v[8:9], v[140:141], v[6:7] op_sel_hi:[1,0]
	v_pk_mul_f32 v[10:11], v[138:139], v[6:7] op_sel_hi:[1,0]
	v_cvt_pk_bf16_f32 v2, v2, v3
	v_cvt_pk_bf16_f32 v3, v4, v5
	s_nop 0
	v_cvt_pk_bf16_f32 v4, v10, v11
	v_cvt_pk_bf16_f32 v5, v8, v9
	v_add_co_u32_e32 v8, vcc, s0, v34
	v_pk_mul_f32 v[10:11], v[132:133], v[6:7] op_sel_hi:[1,0]
	s_nop 0
	v_addc_co_u32_e32 v9, vcc, 0, v35, vcc
	global_store_dwordx4 v[8:9], v[2:5], off
	s_nop 1
	v_pk_mul_f32 v[2:3], v[134:135], v[6:7] op_sel_hi:[1,0]
	v_pk_mul_f32 v[4:5], v[136:137], v[6:7] op_sel_hi:[1,0]
	v_cvt_pk_bf16_f32 v2, v2, v3
	v_pk_mul_f32 v[6:7], v[130:131], v[6:7] op_sel_hi:[1,0]
	v_cvt_pk_bf16_f32 v3, v4, v5
	s_nop 0
	v_cvt_pk_bf16_f32 v4, v6, v7
	v_cvt_pk_bf16_f32 v5, v10, v11
	global_store_dwordx4 v[8:9], v[2:5], off offset:256
	s_nop 1
	v_mov_b32_e32 v2, v19
	v_mov_b32_e32 v3, v20
	v_mov_b32_e32 v19, v21
	v_pk_add_f32 v[2:3], v[2:3], v[18:19]
	s_nop 0
	v_add_f32_e32 v2, v2, v3
	ds_bpermute_b32 v3, v37, v2
	s_waitcnt lgkmcnt(0)
	v_add_f32_e32 v2, v2, v3
	ds_bpermute_b32 v3, v36, v2
	s_waitcnt lgkmcnt(0)
	v_add_f32_e32 v2, v2, v3
	v_fmamk_f32 v2, v2, 0x3b800000, v204
	v_cmp_gt_f32_e32 vcc, s13, v2
	v_mul_f32_e32 v3, 0x4f800000, v2
	s_nop 0
	v_cndmask_b32_e32 v2, v2, v3, vcc
	v_sqrt_f32_e32 v3, v2
	s_nop 0
	v_add_u32_e32 v4, -1, v3
	v_fma_f32 v5, -v4, v3, v2
	v_cmp_ge_f32_e64 s[4:5], 0, v5
	v_add_u32_e32 v5, 1, v3
	s_nop 0
	v_cndmask_b32_e64 v4, v3, v4, s[4:5]
	v_fma_f32 v3, -v5, v3, v2
	v_cmp_lt_f32_e64 s[4:5], 0, v3
	s_nop 1
	v_cndmask_b32_e64 v3, v4, v5, s[4:5]
	v_mul_f32_e32 v4, 0x37800000, v3
	v_cndmask_b32_e32 v3, v3, v4, vcc
	v_cmp_class_f32_e32 vcc, v2, v205
	s_nop 1
	v_cndmask_b32_e32 v2, v3, v2, vcc
	v_div_scale_f32 v3, s[0:1], v2, v2, 1.0
	v_rcp_f32_e32 v4, v3
	s_mov_b32 s0, 0x80000
	v_fma_f32 v5, -v3, v4, 1.0
	v_fmac_f32_e32 v4, v5, v4
	v_div_scale_f32 v5, vcc, 1.0, v2, 1.0
	v_mul_f32_e32 v6, v5, v4
	v_fma_f32 v7, -v3, v6, v5
	v_fmac_f32_e32 v6, v7, v4
	v_fma_f32 v3, -v3, v6, v5
	v_div_fmas_f32 v3, v3, v4, v6
	v_div_fixup_f32 v6, v3, v2, 1.0
	v_pk_mul_f32 v[4:5], v[120:121], v[6:7] op_sel_hi:[1,0]
	v_pk_mul_f32 v[2:3], v[118:119], v[6:7] op_sel_hi:[1,0]
	v_pk_mul_f32 v[8:9], v[116:117], v[6:7] op_sel_hi:[1,0]
	v_pk_mul_f32 v[10:11], v[114:115], v[6:7] op_sel_hi:[1,0]
	v_cvt_pk_bf16_f32 v2, v2, v3
	v_cvt_pk_bf16_f32 v3, v4, v5
	s_nop 0
	v_cvt_pk_bf16_f32 v4, v10, v11
	v_cvt_pk_bf16_f32 v5, v8, v9
	v_add_co_u32_e32 v8, vcc, s0, v34
	v_pk_mul_f32 v[10:11], v[128:129], v[6:7] op_sel_hi:[1,0]
	s_nop 0
	v_addc_co_u32_e32 v9, vcc, 0, v35, vcc
	global_store_dwordx4 v[8:9], v[2:5], off
	s_nop 1
	v_pk_mul_f32 v[2:3], v[122:123], v[6:7] op_sel_hi:[1,0]
	v_pk_mul_f32 v[4:5], v[124:125], v[6:7] op_sel_hi:[1,0]
	v_cvt_pk_bf16_f32 v2, v2, v3
	v_pk_mul_f32 v[6:7], v[126:127], v[6:7] op_sel_hi:[1,0]
	v_cvt_pk_bf16_f32 v3, v4, v5
	s_nop 0
	v_cvt_pk_bf16_f32 v4, v6, v7
	v_cvt_pk_bf16_f32 v5, v10, v11
	global_store_dwordx4 v[8:9], v[2:5], off offset:256
	s_nop 1
	v_mov_b32_e32 v2, v23
	v_mov_b32_e32 v3, v24
	v_mov_b32_e32 v23, v25
	v_pk_add_f32 v[2:3], v[2:3], v[22:23]
	s_nop 0
	v_add_f32_e32 v2, v2, v3
	ds_bpermute_b32 v3, v37, v2
	s_waitcnt lgkmcnt(0)
	v_add_f32_e32 v2, v2, v3
	ds_bpermute_b32 v3, v36, v2
	s_waitcnt lgkmcnt(0)
	v_add_f32_e32 v2, v2, v3
	v_fmamk_f32 v2, v2, 0x3b800000, v204
	v_cmp_gt_f32_e32 vcc, s13, v2
	v_mul_f32_e32 v3, 0x4f800000, v2
	s_nop 0
	v_cndmask_b32_e32 v2, v2, v3, vcc
	v_sqrt_f32_e32 v3, v2
	s_nop 0
	v_add_u32_e32 v4, -1, v3
	v_fma_f32 v5, -v4, v3, v2
	v_cmp_ge_f32_e64 s[4:5], 0, v5
	v_add_u32_e32 v5, 1, v3
	s_nop 0
	v_cndmask_b32_e64 v4, v3, v4, s[4:5]
	v_fma_f32 v3, -v5, v3, v2
	v_cmp_lt_f32_e64 s[4:5], 0, v3
	s_nop 1
	v_cndmask_b32_e64 v3, v4, v5, s[4:5]
	v_mul_f32_e32 v4, 0x37800000, v3
	v_cndmask_b32_e32 v3, v3, v4, vcc
	v_cmp_class_f32_e32 vcc, v2, v205
	s_nop 1
	v_cndmask_b32_e32 v2, v3, v2, vcc
	v_div_scale_f32 v3, s[0:1], v2, v2, 1.0
	v_rcp_f32_e32 v4, v3
	s_mov_b32 s0, 0x90000
	v_fma_f32 v5, -v3, v4, 1.0
	v_fmac_f32_e32 v4, v5, v4
	v_div_scale_f32 v5, vcc, 1.0, v2, 1.0
	v_mul_f32_e32 v6, v5, v4
	v_fma_f32 v7, -v3, v6, v5
	v_fmac_f32_e32 v6, v7, v4
	v_fma_f32 v3, -v3, v6, v5
	v_div_fmas_f32 v3, v3, v4, v6
	v_div_fixup_f32 v6, v3, v2, 1.0
	v_pk_mul_f32 v[4:5], v[104:105], v[6:7] op_sel_hi:[1,0]
	v_pk_mul_f32 v[2:3], v[102:103], v[6:7] op_sel_hi:[1,0]
	v_pk_mul_f32 v[8:9], v[100:101], v[6:7] op_sel_hi:[1,0]
	v_pk_mul_f32 v[10:11], v[98:99], v[6:7] op_sel_hi:[1,0]
	v_cvt_pk_bf16_f32 v2, v2, v3
	v_cvt_pk_bf16_f32 v3, v4, v5
	s_nop 0
	v_cvt_pk_bf16_f32 v4, v10, v11
	v_cvt_pk_bf16_f32 v5, v8, v9
	v_add_co_u32_e32 v8, vcc, s0, v34
	v_pk_mul_f32 v[10:11], v[112:113], v[6:7] op_sel_hi:[1,0]
	s_nop 0
	v_addc_co_u32_e32 v9, vcc, 0, v35, vcc
	global_store_dwordx4 v[8:9], v[2:5], off
	s_nop 1
	v_pk_mul_f32 v[2:3], v[106:107], v[6:7] op_sel_hi:[1,0]
	v_pk_mul_f32 v[4:5], v[108:109], v[6:7] op_sel_hi:[1,0]
	v_cvt_pk_bf16_f32 v2, v2, v3
	v_pk_mul_f32 v[6:7], v[110:111], v[6:7] op_sel_hi:[1,0]
	v_cvt_pk_bf16_f32 v3, v4, v5
	s_nop 0
	v_cvt_pk_bf16_f32 v4, v6, v7
	v_cvt_pk_bf16_f32 v5, v10, v11
	global_store_dwordx4 v[8:9], v[2:5], off offset:256
	s_nop 1
	v_mov_b32_e32 v2, v27
	v_mov_b32_e32 v3, v28
	v_mov_b32_e32 v27, v29
	v_pk_add_f32 v[2:3], v[2:3], v[26:27]
	s_nop 0
	v_add_f32_e32 v2, v2, v3
	ds_bpermute_b32 v3, v37, v2
	s_waitcnt lgkmcnt(0)
	v_add_f32_e32 v2, v2, v3
	ds_bpermute_b32 v3, v36, v2
	s_waitcnt lgkmcnt(0)
	v_add_f32_e32 v2, v2, v3
	v_fmamk_f32 v2, v2, 0x3b800000, v204
	v_cmp_gt_f32_e32 vcc, s13, v2
	v_mul_f32_e32 v3, 0x4f800000, v2
	s_nop 0
	v_cndmask_b32_e32 v2, v2, v3, vcc
	v_sqrt_f32_e32 v3, v2
	s_nop 0
	v_add_u32_e32 v4, -1, v3
	v_fma_f32 v5, -v4, v3, v2
	v_cmp_ge_f32_e64 s[4:5], 0, v5
	v_add_u32_e32 v5, 1, v3
	s_nop 0
	v_cndmask_b32_e64 v4, v3, v4, s[4:5]
	v_fma_f32 v3, -v5, v3, v2
	v_cmp_lt_f32_e64 s[4:5], 0, v3
	s_nop 1
	v_cndmask_b32_e64 v3, v4, v5, s[4:5]
	v_mul_f32_e32 v4, 0x37800000, v3
	v_cndmask_b32_e32 v3, v3, v4, vcc
	v_cmp_class_f32_e32 vcc, v2, v205
	s_nop 1
	v_cndmask_b32_e32 v2, v3, v2, vcc
	v_div_scale_f32 v3, s[0:1], v2, v2, 1.0
	v_rcp_f32_e32 v4, v3
	s_mov_b32 s0, 0xa0000
	v_fma_f32 v5, -v3, v4, 1.0
	v_fmac_f32_e32 v4, v5, v4
	v_div_scale_f32 v5, vcc, 1.0, v2, 1.0
	v_mul_f32_e32 v6, v5, v4
	v_fma_f32 v7, -v3, v6, v5
	v_fmac_f32_e32 v6, v7, v4
	v_fma_f32 v3, -v3, v6, v5
	v_div_fmas_f32 v3, v3, v4, v6
	v_div_fixup_f32 v6, v3, v2, 1.0
	v_pk_mul_f32 v[4:5], v[88:89], v[6:7] op_sel_hi:[1,0]
	v_pk_mul_f32 v[2:3], v[86:87], v[6:7] op_sel_hi:[1,0]
	v_pk_mul_f32 v[8:9], v[84:85], v[6:7] op_sel_hi:[1,0]
	v_pk_mul_f32 v[10:11], v[82:83], v[6:7] op_sel_hi:[1,0]
	v_cvt_pk_bf16_f32 v2, v2, v3
	v_cvt_pk_bf16_f32 v3, v4, v5
	s_nop 0
	v_cvt_pk_bf16_f32 v4, v10, v11
	v_cvt_pk_bf16_f32 v5, v8, v9
	v_add_co_u32_e32 v8, vcc, s0, v34
	v_pk_mul_f32 v[10:11], v[96:97], v[6:7] op_sel_hi:[1,0]
	s_nop 0
	v_addc_co_u32_e32 v9, vcc, 0, v35, vcc
	global_store_dwordx4 v[8:9], v[2:5], off
	s_nop 1
	v_pk_mul_f32 v[2:3], v[90:91], v[6:7] op_sel_hi:[1,0]
	v_pk_mul_f32 v[4:5], v[92:93], v[6:7] op_sel_hi:[1,0]
	v_cvt_pk_bf16_f32 v2, v2, v3
	v_pk_mul_f32 v[6:7], v[94:95], v[6:7] op_sel_hi:[1,0]
	v_cvt_pk_bf16_f32 v3, v4, v5
	s_nop 0
	v_cvt_pk_bf16_f32 v4, v6, v7
	v_cvt_pk_bf16_f32 v5, v10, v11
	global_store_dwordx4 v[8:9], v[2:5], off offset:256
	s_nop 1
	v_mov_b32_e32 v2, v31
	v_mov_b32_e32 v3, v32
	v_mov_b32_e32 v31, v33
	v_pk_add_f32 v[2:3], v[2:3], v[30:31]
	s_nop 0
	v_add_f32_e32 v2, v2, v3
	ds_bpermute_b32 v3, v37, v2
	s_waitcnt lgkmcnt(0)
	v_add_f32_e32 v2, v2, v3
	ds_bpermute_b32 v3, v36, v2
	s_waitcnt lgkmcnt(0)
	v_add_f32_e32 v2, v2, v3
	v_fmamk_f32 v2, v2, 0x3b800000, v204
	v_cmp_gt_f32_e32 vcc, s13, v2
	v_mul_f32_e32 v3, 0x4f800000, v2
	s_nop 0
	v_cndmask_b32_e32 v2, v2, v3, vcc
	v_sqrt_f32_e32 v3, v2
	s_nop 0
	v_add_u32_e32 v4, -1, v3
	v_fma_f32 v5, -v4, v3, v2
	v_cmp_ge_f32_e64 s[4:5], 0, v5
	v_add_u32_e32 v5, 1, v3
	s_nop 0
	v_cndmask_b32_e64 v4, v3, v4, s[4:5]
	v_fma_f32 v3, -v5, v3, v2
	v_cmp_lt_f32_e64 s[4:5], 0, v3
	s_nop 1
	v_cndmask_b32_e64 v3, v4, v5, s[4:5]
	v_mul_f32_e32 v4, 0x37800000, v3
	v_cndmask_b32_e32 v3, v3, v4, vcc
	v_cmp_class_f32_e32 vcc, v2, v205
	s_mov_b64 s[4:5], -1
	s_nop 0
	v_cndmask_b32_e32 v2, v3, v2, vcc
	v_div_scale_f32 v3, s[0:1], v2, v2, 1.0
	v_rcp_f32_e32 v4, v3
	s_mov_b32 s0, 0xb0000
	v_fma_f32 v5, -v3, v4, 1.0
	v_fmac_f32_e32 v4, v5, v4
	v_div_scale_f32 v5, vcc, 1.0, v2, 1.0
	v_mul_f32_e32 v6, v5, v4
	v_fma_f32 v7, -v3, v6, v5
	v_fmac_f32_e32 v6, v7, v4
	v_fma_f32 v3, -v3, v6, v5
	v_div_fmas_f32 v3, v3, v4, v6
	v_div_fixup_f32 v6, v3, v2, 1.0
	v_pk_mul_f32 v[4:5], v[72:73], v[6:7] op_sel_hi:[1,0]
	v_pk_mul_f32 v[2:3], v[70:71], v[6:7] op_sel_hi:[1,0]
	v_pk_mul_f32 v[8:9], v[68:69], v[6:7] op_sel_hi:[1,0]
	v_pk_mul_f32 v[10:11], v[66:67], v[6:7] op_sel_hi:[1,0]
	v_cvt_pk_bf16_f32 v2, v2, v3
	v_cvt_pk_bf16_f32 v3, v4, v5
	s_nop 0
	v_cvt_pk_bf16_f32 v4, v10, v11
	v_cvt_pk_bf16_f32 v5, v8, v9
	v_add_co_u32_e32 v8, vcc, s0, v34
	v_pk_mul_f32 v[10:11], v[80:81], v[6:7] op_sel_hi:[1,0]
	s_nop 0
	v_addc_co_u32_e32 v9, vcc, 0, v35, vcc
	global_store_dwordx4 v[8:9], v[2:5], off
	s_and_b64 vcc, exec, s[2:3]
	s_nop 0
	v_pk_mul_f32 v[4:5], v[76:77], v[6:7] op_sel_hi:[1,0]
	v_pk_mul_f32 v[2:3], v[74:75], v[6:7] op_sel_hi:[1,0]
	v_pk_mul_f32 v[6:7], v[78:79], v[6:7] op_sel_hi:[1,0]
	v_cvt_pk_bf16_f32 v2, v2, v3
	v_cvt_pk_bf16_f32 v3, v4, v5
	s_nop 0
	v_cvt_pk_bf16_f32 v4, v6, v7
	v_cvt_pk_bf16_f32 v5, v10, v11
	global_store_dwordx4 v[8:9], v[2:5], off offset:256
	s_cbranch_vccnz .LBB0_851
	s_andn2_b64 vcc, exec, s[8:9]
	s_cbranch_vccnz .LBB0_850
	s_barrier
	s_branch .LBB0_850
.LBB0_873:
	s_waitcnt vmcnt(0)
	v_readlane_b32 s34, v255, 46
	v_readlane_b32 s35, v255, 47
	v_readlane_b32 s37, v255, 48
	s_barrier
